# attention-A tile loop specialised in two copies chosen once per unit: side-work units (fixed counted wait, no per-tile activity tests) and the unit without side work (no side-work code); -8 instr per
# speedup vs baseline: 1.0105x; 1.0010x over previous
.Lpro_noconv:
	s_cmp_lg_u64 s[12:13], 0
	s_cselect_b64 s[54:55], -1, 0
	s_cmp_lt_u32 s0, 2
	s_mov_b32 s0, 0x3f400000
	s_cselect_b64 s[52:53], -1, 0
	s_mov_b32 s8, s9
	v_mfma_scale_f32_32x32x64_f8f6f4 v[16:31], v[12:17], v[182:187], 0, v217, v216 op_sel_hi:[0,0,0] cbsz:2 blgp:2
	s_nop 4
	v_max_f32_e32 v52, v33, v33
	v_max_f32_e32 v53, v32, v32
	v_max_f32_e32 v52, v53, v52
	v_max3_f32 v52, v52, v34, v35
	v_max3_f32 v52, v52, v36, v37
	v_max3_f32 v52, v52, v38, v39
	v_max3_f32 v52, v52, v40, v41
	v_mfma_scale_f32_32x32x64_f8f6f4 v[16:31], v[58:63], v[176:181], v[16:31], v217, v216 op_sel_hi:[0,0,0] cbsz:2 blgp:2
	v_max3_f32 v52, v52, v42, v43
	v_max3_f32 v52, v52, v44, v45
	v_max3_f32 v52, v52, v46, v47
	s_mov_b32 s10, s9
	s_mov_b32 s11, s9
	s_mov_b32 s12, s9
	s_mov_b32 s13, s9
	s_nop 4
	v_max3_f32 v52, v52, v16, v17
	v_max3_f32 v52, v52, v18, v19
	v_max3_f32 v52, v52, v20, v21
	v_max3_f32 v52, v52, v22, v23
	v_max3_f32 v52, v52, v24, v25
	v_max3_f32 v52, v52, v26, v27
	v_max3_f32 v52, v52, v28, v29
	v_max3_f32 v52, v52, v30, v31
	v_mov_b32_e32 v53, v52
	s_nop 1
	v_permlane32_swap_b32_e32 v52, v53
	v_max_f32_e32 v53, v53, v53
	v_max_f32_e32 v52, v52, v52
	v_max_f32_e32 v52, v52, v53
	v_add_f32_e32 v53, 0x7149f2ca, v52
	v_cmp_ge_f32_e32 vcc, s0, v53
	v_max_f32_e32 v52, 0xf149f2ca, v52
	s_cmp_lg_u64 vcc, exec
	v_add_f32_e32 v52, 2.0, v52
	s_cselect_b64 vcc, -1, 0
	v_cndmask_b32_e32 v52, v219, v52, vcc
	v_add_f32_e32 v53, -4.0, v52
	s_lshl_b32 s0, s46, 2
	v_sub_f32_e32 v32, v32, v53
	v_sub_f32_e32 v33, v33, v53
	v_sub_f32_e32 v34, v34, v53
	v_sub_f32_e32 v35, v35, v53
	v_sub_f32_e32 v36, v36, v53
	v_sub_f32_e32 v37, v37, v53
	v_sub_f32_e32 v38, v38, v53
	v_sub_f32_e32 v39, v39, v53
	v_sub_f32_e32 v40, v40, v53
	v_sub_f32_e32 v41, v41, v53
	v_sub_f32_e32 v42, v42, v53
	v_sub_f32_e32 v43, v43, v53
	v_sub_f32_e32 v44, v44, v53
	v_sub_f32_e32 v45, v45, v53
	v_sub_f32_e32 v46, v46, v53
	v_sub_f32_e32 v47, v47, v53
	s_add_i32 s0, s0, 0
	s_mov_b32 s14, s9
	s_mov_b32 s15, s9
	s_mov_b32 s16, s9
	s_mov_b32 s17, s9
	s_mov_b32 s18, s9
	s_mov_b32 s19, s9
	s_mov_b32 s20, s9
	s_mov_b32 s21, s9
	s_mov_b32 s22, s9
	s_mov_b32 s23, s9
	v_mov_b64_e32 v[0:1], s[8:9]
	v_exp_f32_e32 v144, v32
	v_exp_f32_e32 v145, v33
	v_exp_f32_e32 v146, v34
	v_exp_f32_e32 v147, v35
	v_exp_f32_e32 v148, v36
	v_exp_f32_e32 v149, v37
	v_exp_f32_e32 v150, v38
	v_exp_f32_e32 v151, v39
	v_exp_f32_e32 v152, v40
	v_exp_f32_e32 v153, v41
	v_exp_f32_e32 v154, v42
	v_exp_f32_e32 v155, v43
	v_exp_f32_e32 v156, v44
	v_exp_f32_e32 v157, v45
	v_exp_f32_e32 v158, v46
	v_exp_f32_e32 v159, v47
	s_add_i32 s0, s0, 0x1c800
	v_mov_b64_e32 v[2:3], s[10:11]
	v_mov_b64_e32 v[4:5], s[12:13]
	v_mov_b64_e32 v[6:7], s[14:15]
	v_mov_b64_e32 v[8:9], s[16:17]
	v_mov_b64_e32 v[10:11], s[18:19]
	v_mov_b64_e32 v[12:13], s[20:21]
	v_mov_b64_e32 v[14:15], s[22:23]
	v_sub_f32_e32 v128, v16, v53
	s_and_b64 s[10:11], s[52:53], exec
	v_lshlrev_b32_e32 v16, 7, v48
	v_sub_f32_e32 v80, 4.0, v52
	v_sub_f32_e32 v143, v31, v53
	v_sub_f32_e32 v142, v30, v53
	v_sub_f32_e32 v141, v29, v53
	v_sub_f32_e32 v140, v28, v53
	v_sub_f32_e32 v139, v27, v53
	v_sub_f32_e32 v138, v26, v53
	v_sub_f32_e32 v137, v25, v53
	v_sub_f32_e32 v136, v24, v53
	v_sub_f32_e32 v135, v23, v53
	v_sub_f32_e32 v134, v22, v53
	v_sub_f32_e32 v133, v21, v53
	v_sub_f32_e32 v132, v20, v53
	v_sub_f32_e32 v131, v19, v53
	v_sub_f32_e32 v130, v18, v53
	v_sub_f32_e32 v129, v17, v53
	s_cselect_b32 s14, 23, 22
	v_add3_u32 v164, s85, v16, v51
	s_add_u32 s10, s78, s4
	v_add_u32_e32 v174, v49, v50
	v_mov_b64_e32 v[62:63], v[14:15]
	v_mov_b64_e32 v[46:47], v[14:15]
	v_mov_b64_e32 v[30:31], v[14:15]
	v_mov_b64_e32 v[78:79], v[14:15]
	s_mov_b32 s1, 2
	s_mov_b32 s57, 1
	s_mov_b32 s27, -2
	v_mov_b32_e32 v81, v80
	v_mov_b32_e32 v82, v80
	v_mov_b32_e32 v83, v80
	v_mov_b32_e32 v84, v80
	v_mov_b32_e32 v85, v80
	v_mov_b32_e32 v86, v80
	v_mov_b32_e32 v87, v80
	v_mov_b32_e32 v88, v80
	v_mov_b32_e32 v89, v80
	v_mov_b32_e32 v90, v80
	v_mov_b32_e32 v91, v80
	v_mov_b32_e32 v92, v80
	v_mov_b32_e32 v93, v80
	v_mov_b32_e32 v94, v80
	v_mov_b32_e32 v95, v80
	s_mov_b32 s15, 0
	v_mov_b32_e32 v165, v167
	s_addc_u32 s11, s79, s5
	v_mov_b32_e32 v175, v167
	v_mov_b64_e32 v[60:61], v[12:13]
	v_mov_b64_e32 v[58:59], v[10:11]
	v_mov_b64_e32 v[56:57], v[8:9]
	v_mov_b64_e32 v[54:55], v[6:7]
	v_mov_b64_e32 v[52:53], v[4:5]
	v_mov_b64_e32 v[50:51], v[2:3]
	v_mov_b64_e32 v[48:49], v[0:1]
	v_mov_b64_e32 v[44:45], v[12:13]
	v_mov_b64_e32 v[42:43], v[10:11]
	v_mov_b64_e32 v[40:41], v[8:9]
	v_mov_b64_e32 v[38:39], v[6:7]
	v_mov_b64_e32 v[36:37], v[4:5]
	v_mov_b64_e32 v[34:35], v[2:3]
	v_mov_b64_e32 v[32:33], v[0:1]
	v_mov_b64_e32 v[28:29], v[12:13]
	v_mov_b64_e32 v[26:27], v[10:11]
	v_mov_b64_e32 v[24:25], v[8:9]
	v_mov_b64_e32 v[22:23], v[6:7]
	v_mov_b64_e32 v[20:21], v[4:5]
	v_mov_b64_e32 v[18:19], v[2:3]
	v_mov_b64_e32 v[16:17], v[0:1]
	s_mov_b32 s16, 2
	v_mov_b64_e32 v[76:77], v[12:13]
	v_mov_b64_e32 v[74:75], v[10:11]
	v_mov_b64_e32 v[72:73], v[8:9]
	v_mov_b64_e32 v[70:71], v[6:7]
	v_mov_b64_e32 v[68:69], v[4:5]
	v_mov_b64_e32 v[66:67], v[2:3]
	v_mov_b64_e32 v[64:65], v[0:1]
	v_mbcnt_lo_u32_b32 v200, -1, 0
	v_mbcnt_hi_u32_b32 v200, -1, v200
	v_lshrrev_b32_e32 v201, 3, v200
	v_mul_lo_u32 v201, v201, s56
	v_lshlrev_b32_e32 v200, 4, v200
	v_and_b32_e32 v200, 0x70, v200
	v_lshl_or_b32 v214, v201, 2, v200
	v_mov_b32_e32 v215, v214
	s_mov_b64 s[98:99], s[58:59]
	s_add_i32 s100, s66, 0xc800
	s_lshl_b32 s101, s56, 5
	s_movk_i32 s15, 0x70
	ds_read_b128 v[228:231], v223 offset:8192
	ds_read_b64 v[232:233], v224 offset:8192
	ds_read_b128 v[234:237], v223 offset:12288
	ds_read_b64 v[238:239], v224 offset:12288
	ds_read_b128 v[240:243], v221 offset:8192
	ds_read_b64 v[244:245], v222 offset:8192
	ds_read_b128 v[246:249], v221 offset:12288
	ds_read_b64 v[250:251], v222 offset:12288
	v_mbcnt_lo_u32_b32 v200, -1, 0
	v_mbcnt_hi_u32_b32 v200, -1, v200
	v_and_b32_e32 v201, 7, v200
	v_ashrrev_i32_e32 v202, 3, v200
	v_lshlrev_b32_e32 v203, 2, v200
	v_lshl_add_u32 v204, v201, 10, s66
	v_lshlrev_b32_e32 v205, 2, v202
	v_and_b32_e32 v205, 12, v205
	v_add_u32_e32 v204, 0xc800, v204
	v_add_u32_e32 v204, v204, v205
	v_add_u32_e32 v206, v202, v203
	v_add_u32_e32 v207, 8, v206
	v_add_u32_e32 v208, 16, v206
	v_add_u32_e32 v209, 24, v206
	v_and_b32_e32 v206, 28, v206
	v_and_b32_e32 v207, 28, v207
	v_and_b32_e32 v208, 28, v208
	v_and_b32_e32 v209, 28, v209
	v_lshl_add_u32 v206, v206, 2, v204
	v_lshl_add_u32 v207, v207, 2, v204
	v_lshl_add_u32 v208, v208, 2, v204
	v_lshl_add_u32 v209, v209, 2, v204
	v_mul_u32_u24_e32 v210, s48, v202
	v_lshl_add_u32 v210, v201, 3, v210
	v_lshl_add_u32 v211, v201, 5, s0
	v_lshl_add_u32 v205, v200, 4, s89
	ds_write_b128 v205, v[206:209] offset:16384
	ds_write_b64 v205, v[210:211] offset:40960
	s_add_u32 s16, s10, 0x74802000
	s_addc_u32 s17, s11, 0
	s_add_u32 s10, s10, 0x74006000
	s_addc_u32 s11, s11, 0
	s_cmp_lg_u64 s[60:61], 0
	s_cbranch_scc1 .Lattn_top_n
.Lattn_top:
	s_waitcnt vmcnt(1) lgkmcnt(0)
.LBB0_417:
	s_add_i32 m0, s89, 0x2000
	s_barrier
	global_load_lds_dwordx4 v164, s[10:11]
	v_add_u32_e32 v164, 0x2000, v164
	s_add_i32 m0, s89, 0x8000
	s_add_u32 s98, s98, s101
	global_load_lds_dwordx4 v174, s[16:17]
	v_add_u32_e32 v174, 0x2000, v174
	s_addc_u32 s99, s99, 0
	s_add_i32 s100, s100, 0x400
	s_mov_b32 m0, s100
	v_add_u32_e32 v96, -16, v215
	v_bfi_b32 v215, s15, v96, v215
	global_load_lds_dwordx4 v215, s[98:99] nt

.LBB0_424:
	v_exp_f32_e32 v112, v112
	v_exp_f32_e32 v113, v113
	v_exp_f32_e32 v114, v114
	v_exp_f32_e32 v115, v115
	v_exp_f32_e32 v116, v116
	v_exp_f32_e32 v117, v117
	v_exp_f32_e32 v118, v118
	v_exp_f32_e32 v119, v119
	v_exp_f32_e32 v120, v120
	v_exp_f32_e32 v121, v121
	v_exp_f32_e32 v122, v122
	v_exp_f32_e32 v123, v123
	v_exp_f32_e32 v124, v124
	v_exp_f32_e32 v125, v125
	v_exp_f32_e32 v126, v126
	v_exp_f32_e32 v127, v127
	s_waitcnt vmcnt(1) lgkmcnt(0)
.LBB0_428:
	s_mov_b32 m0, s89
	s_barrier
	global_load_lds_dwordx4 v164, s[10:11]
	v_add_u32_e32 v164, 0x2000, v164
	s_add_i32 m0, s89, 0x6000
	s_bfe_u32 s4, s1, 0x30000
	global_load_lds_dwordx4 v174, s[16:17]
	v_add_u32_e32 v174, 0x2000, v174
	s_cbranch_scc0 .LBB0_432
	s_add_u32 s98, s98, s101
	s_addc_u32 s99, s99, 0
	s_add_i32 s100, s100, 0x400
	s_mov_b32 m0, s100
	v_add_u32_e32 v128, -16, v215
	v_bfi_b32 v215, s15, v128, v215
	global_load_lds_dwordx4 v215, s[98:99] nt

.Lfin_done:
	s_lshl_b64 s[98:99], s[8:9], 24
	s_add_u32 s98, s58, s98
	s_addc_u32 s99, s59, s99
	s_add_i32 s100, s66, 0xc800
	v_mov_b32_e32 v215, v214
	s_mov_b32 m0, s100
	s_nop 0
	global_load_lds_dwordx4 v215, s[98:99] nt
	s_branch .LBB0_437
.LBB0_420:
	v_cmp_gt_f32_e32 vcc, 1.0, v166
	s_cbranch_vccz .LBB0_424
	v_mbcnt_lo_u32_b32 v128, -1, 0
	v_mbcnt_hi_u32_b32 v128, -1, v128
	s_nop 0
	v_cmp_gt_u32_e32 vcc, 32, v128
	s_and_saveexec_b64 s[12:13], vcc
	v_lshl_add_u32 v129, v128, 2, s86
	ds_write_b32 v129, v166 offset:49152
	s_or_b64 exec, exec, s[12:13]
	v_ashrrev_i32_e32 v128, 3, v128
	v_lshlrev_b32_e32 v128, 2, v128
	v_and_b32_e32 v128, -16, v128
	s_waitcnt lgkmcnt(0)
	v_add_u32_e32 v140, s86, v128
	ds_read_b128 v[128:131], v140 offset:49248
	ds_read_b128 v[132:135], v140 offset:49216
	ds_read_b128 v[136:139], v140 offset:49184
	ds_read_b128 v[140:143], v140 offset:49152
	s_waitcnt lgkmcnt(0)
	v_pk_mul_f32 v[12:13], v[12:13], v[128:129]
	v_pk_mul_f32 v[8:9], v[8:9], v[132:133]
	v_pk_mul_f32 v[4:5], v[4:5], v[136:137]
	v_pk_mul_f32 v[14:15], v[14:15], v[130:131]
	v_pk_mul_f32 v[10:11], v[10:11], v[134:135]
	v_pk_mul_f32 v[6:7], v[6:7], v[138:139]
	v_pk_mul_f32 v[2:3], v[2:3], v[142:143]
	v_pk_mul_f32 v[0:1], v[0:1], v[140:141]
	v_pk_mul_f32 v[60:61], v[60:61], v[128:129]
	v_pk_mul_f32 v[56:57], v[56:57], v[132:133]
	v_pk_mul_f32 v[52:53], v[52:53], v[136:137]
	v_pk_mul_f32 v[62:63], v[62:63], v[130:131]
	v_pk_mul_f32 v[58:59], v[58:59], v[134:135]
	v_pk_mul_f32 v[54:55], v[54:55], v[138:139]
	v_pk_mul_f32 v[50:51], v[50:51], v[142:143]
	v_pk_mul_f32 v[48:49], v[48:49], v[140:141]
	v_pk_mul_f32 v[44:45], v[44:45], v[128:129]
	v_pk_mul_f32 v[40:41], v[40:41], v[132:133]
	v_pk_mul_f32 v[36:37], v[36:37], v[136:137]
	v_pk_mul_f32 v[46:47], v[46:47], v[130:131]
	v_pk_mul_f32 v[42:43], v[42:43], v[134:135]
	v_pk_mul_f32 v[38:39], v[38:39], v[138:139]
	v_pk_mul_f32 v[34:35], v[34:35], v[142:143]
	v_pk_mul_f32 v[32:33], v[32:33], v[140:141]
	v_pk_mul_f32 v[28:29], v[28:29], v[128:129]
	v_pk_mul_f32 v[24:25], v[24:25], v[132:133]
	v_pk_mul_f32 v[20:21], v[20:21], v[136:137]
	v_pk_mul_f32 v[30:31], v[30:31], v[130:131]
	v_pk_mul_f32 v[26:27], v[26:27], v[134:135]
	v_pk_mul_f32 v[22:23], v[22:23], v[138:139]
	v_pk_mul_f32 v[18:19], v[18:19], v[142:143]
	v_pk_mul_f32 v[16:17], v[16:17], v[140:141]
	v_pk_mul_f32 v[76:77], v[76:77], v[128:129]
	v_pk_mul_f32 v[72:73], v[72:73], v[132:133]
	v_pk_mul_f32 v[68:69], v[68:69], v[136:137]
	v_pk_mul_f32 v[78:79], v[78:79], v[130:131]
	v_pk_mul_f32 v[74:75], v[74:75], v[134:135]
	v_pk_mul_f32 v[70:71], v[70:71], v[138:139]
	v_pk_mul_f32 v[66:67], v[66:67], v[142:143]
	v_pk_mul_f32 v[64:65], v[64:65], v[140:141]
	s_branch .LBB0_424

.LBB0_417_n:
	s_add_i32 m0, s89, 0x2000
	s_barrier
	global_load_lds_dwordx4 v164, s[10:11]
	v_add_u32_e32 v164, 0x2000, v164
	s_add_i32 m0, s89, 0x8000
	s_nop 0
	global_load_lds_dwordx4 v174, s[16:17]
	v_add_u32_e32 v174, 0x2000, v174

.LBB0_424_n:
	v_exp_f32_e32 v112, v112
	v_exp_f32_e32 v113, v113
	v_exp_f32_e32 v114, v114
	v_exp_f32_e32 v115, v115
	v_exp_f32_e32 v116, v116
	v_exp_f32_e32 v117, v117
	v_exp_f32_e32 v118, v118
	v_exp_f32_e32 v119, v119
	v_exp_f32_e32 v120, v120
	v_exp_f32_e32 v121, v121
	v_exp_f32_e32 v122, v122
	v_exp_f32_e32 v123, v123
	v_exp_f32_e32 v124, v124
	v_exp_f32_e32 v125, v125
	v_exp_f32_e32 v126, v126
	v_exp_f32_e32 v127, v127
	s_waitcnt vmcnt(0) lgkmcnt(0)
.LBB0_428_n:
	s_mov_b32 m0, s89
	s_barrier
	global_load_lds_dwordx4 v164, s[10:11]
	v_add_u32_e32 v164, 0x2000, v164
	s_add_i32 m0, s89, 0x6000
	s_nop 0
	global_load_lds_dwordx4 v174, s[16:17]
	v_add_u32_e32 v174, 0x2000, v174

.LBB0_445_n:
	v_mov_b32_e32 v213, v212
	s_nop 1
	v_permlane32_swap_b32_e32 v212, v213
	v_max_f32_e32 v213, v213, v213
	v_max_f32_e32 v212, v212, v212
	v_max_f32_e32 v212, v212, v213
	v_add_f32_e32 v166, -4.0, v212
	v_add_f32_e32 v166, 1.0, v166
	v_max_f32_e32 v212, 0, v166
	v_exp_f32_e64 v166, -v212
	v_pk_add_f32 v[144:145], v[144:145], v[212:213] op_sel_hi:[1,0] neg_lo:[0,1] neg_hi:[0,1]
	v_pk_add_f32 v[146:147], v[146:147], v[212:213] op_sel_hi:[1,0] neg_lo:[0,1] neg_hi:[0,1]
	v_pk_add_f32 v[148:149], v[148:149], v[212:213] op_sel_hi:[1,0] neg_lo:[0,1] neg_hi:[0,1]
	v_pk_add_f32 v[150:151], v[150:151], v[212:213] op_sel_hi:[1,0] neg_lo:[0,1] neg_hi:[0,1]
	v_pk_add_f32 v[152:153], v[152:153], v[212:213] op_sel_hi:[1,0] neg_lo:[0,1] neg_hi:[0,1]
	v_pk_add_f32 v[154:155], v[154:155], v[212:213] op_sel_hi:[1,0] neg_lo:[0,1] neg_hi:[0,1]
	v_pk_add_f32 v[156:157], v[156:157], v[212:213] op_sel_hi:[1,0] neg_lo:[0,1] neg_hi:[0,1]
	v_pk_add_f32 v[158:159], v[158:159], v[212:213] op_sel_hi:[1,0] neg_lo:[0,1] neg_hi:[0,1]
	v_sub_f32_e32 v143, v143, v212
	v_sub_f32_e32 v142, v142, v212
	v_sub_f32_e32 v141, v141, v212
	v_sub_f32_e32 v140, v140, v212
	v_sub_f32_e32 v139, v139, v212
	v_sub_f32_e32 v138, v138, v212
	v_sub_f32_e32 v137, v137, v212
	v_sub_f32_e32 v136, v136, v212
	v_sub_f32_e32 v135, v135, v212
	v_sub_f32_e32 v134, v134, v212
	v_sub_f32_e32 v133, v133, v212
	v_sub_f32_e32 v132, v132, v212
	v_sub_f32_e32 v131, v131, v212
	v_sub_f32_e32 v130, v130, v212
	v_sub_f32_e32 v129, v129, v212
	v_sub_f32_e32 v128, v128, v212
	v_sub_f32_e32 v95, v95, v212
	v_sub_f32_e32 v94, v94, v212
	v_sub_f32_e32 v93, v93, v212
	v_sub_f32_e32 v92, v92, v212
	v_sub_f32_e32 v91, v91, v212
	v_sub_f32_e32 v90, v90, v212
	v_sub_f32_e32 v89, v89, v212
	v_sub_f32_e32 v88, v88, v212
	v_sub_f32_e32 v87, v87, v212
	v_sub_f32_e32 v86, v86, v212
	v_sub_f32_e32 v85, v85, v212
	v_sub_f32_e32 v84, v84, v212
	v_sub_f32_e32 v83, v83, v212
	v_sub_f32_e32 v82, v82, v212
	v_sub_f32_e32 v81, v81, v212
	v_sub_f32_e32 v80, v80, v212
	s_branch .LBB0_438_n
.LBB0_420_n:
	v_cmp_gt_f32_e32 vcc, 1.0, v166
	s_cbranch_vccz .LBB0_424_n
	v_mbcnt_lo_u32_b32 v128, -1, 0
	v_mbcnt_hi_u32_b32 v128, -1, v128
	s_nop 0
	v_cmp_gt_u32_e32 vcc, 32, v128
	s_and_saveexec_b64 s[12:13], vcc
	v_lshl_add_u32 v129, v128, 2, s86
	ds_write_b32 v129, v166 offset:49152
	s_or_b64 exec, exec, s[12:13]
	v_ashrrev_i32_e32 v128, 3, v128
	v_lshlrev_b32_e32 v128, 2, v128
	v_and_b32_e32 v128, -16, v128
	s_waitcnt lgkmcnt(0)
	v_add_u32_e32 v140, s86, v128
	ds_read_b128 v[128:131], v140 offset:49248
	ds_read_b128 v[132:135], v140 offset:49216
	ds_read_b128 v[136:139], v140 offset:49184
	ds_read_b128 v[140:143], v140 offset:49152
	s_waitcnt lgkmcnt(0)
	v_pk_mul_f32 v[12:13], v[12:13], v[128:129]
	v_pk_mul_f32 v[8:9], v[8:9], v[132:133]
	v_pk_mul_f32 v[4:5], v[4:5], v[136:137]
	v_pk_mul_f32 v[14:15], v[14:15], v[130:131]
	v_pk_mul_f32 v[10:11], v[10:11], v[134:135]
	v_pk_mul_f32 v[6:7], v[6:7], v[138:139]
	v_pk_mul_f32 v[2:3], v[2:3], v[142:143]
	v_pk_mul_f32 v[0:1], v[0:1], v[140:141]
	v_pk_mul_f32 v[60:61], v[60:61], v[128:129]
	v_pk_mul_f32 v[56:57], v[56:57], v[132:133]
	v_pk_mul_f32 v[52:53], v[52:53], v[136:137]
	v_pk_mul_f32 v[62:63], v[62:63], v[130:131]
	v_pk_mul_f32 v[58:59], v[58:59], v[134:135]
	v_pk_mul_f32 v[54:55], v[54:55], v[138:139]
	v_pk_mul_f32 v[50:51], v[50:51], v[142:143]
	v_pk_mul_f32 v[48:49], v[48:49], v[140:141]
	v_pk_mul_f32 v[44:45], v[44:45], v[128:129]
	v_pk_mul_f32 v[40:41], v[40:41], v[132:133]
	v_pk_mul_f32 v[36:37], v[36:37], v[136:137]
	v_pk_mul_f32 v[46:47], v[46:47], v[130:131]
	v_pk_mul_f32 v[42:43], v[42:43], v[134:135]
	v_pk_mul_f32 v[38:39], v[38:39], v[138:139]
	v_pk_mul_f32 v[34:35], v[34:35], v[142:143]
	v_pk_mul_f32 v[32:33], v[32:33], v[140:141]
	v_pk_mul_f32 v[28:29], v[28:29], v[128:129]
	v_pk_mul_f32 v[24:25], v[24:25], v[132:133]
	v_pk_mul_f32 v[20:21], v[20:21], v[136:137]
	v_pk_mul_f32 v[30:31], v[30:31], v[130:131]
	v_pk_mul_f32 v[26:27], v[26:27], v[134:135]
	v_pk_mul_f32 v[22:23], v[22:23], v[138:139]
	v_pk_mul_f32 v[18:19], v[18:19], v[142:143]
	v_pk_mul_f32 v[16:17], v[16:17], v[140:141]
	v_pk_mul_f32 v[76:77], v[76:77], v[128:129]
	v_pk_mul_f32 v[72:73], v[72:73], v[132:133]
	v_pk_mul_f32 v[68:69], v[68:69], v[136:137]
	v_pk_mul_f32 v[78:79], v[78:79], v[130:131]
	v_pk_mul_f32 v[74:75], v[74:75], v[134:135]
	v_pk_mul_f32 v[70:71], v[70:71], v[138:139]
	v_pk_mul_f32 v[66:67], v[66:67], v[142:143]
	v_pk_mul_f32 v[64:65], v[64:65], v[140:141]
	s_branch .LBB0_424_n
